# attention: leaner DMA issue block; next-tile row sums accumulated inside the second half of the PV MFMAs
# baseline (speedup 1.0000x reference)
.LBB0_396:
	s_add_i32 m0, s25, s96
	s_add_i32 s0, s25, s97
	global_load_lds_dwordx4 v[160:161], off
	s_addk_i32 m0, 0x2000
	s_add_i32 s3, s0, 0x4000
	global_load_lds_dwordx4 v[158:159], off
	s_mov_b32 m0, s3
	s_addk_i32 s0, 0x4400
	global_load_lds_dwordx4 v[156:157], off
	s_mov_b32 m0, s0
	s_nop 0
	global_load_lds_dwordx4 v[154:155], off

.LBB0_435:
	s_add_i32 s0, s73, 0
	v_add_u32_e32 v152, s0, v175
	v_add_u32_e32 v177, s0, v174
	v_add_u32_e32 v194, s0, v173
	v_add_u32_e32 v195, s0, v172
	ds_read_b64_tr_b16 v[100:101], v152 offset:16384
	ds_read_b64_tr_b16 v[102:103], v177 offset:16384
	ds_read_b64_tr_b16 v[106:107], v177 offset:20480
	ds_read_b64_tr_b16 v[104:105], v152 offset:20480
	ds_read_b64_tr_b16 v[108:109], v194 offset:16384
	ds_read_b64_tr_b16 v[110:111], v195 offset:16384
	ds_read_b64_tr_b16 v[114:115], v195 offset:20480
	ds_read_b64_tr_b16 v[112:113], v194 offset:20480
	s_waitcnt lgkmcnt(8)
	v_mfma_f32_32x32x16_bf16 v[20:35], v[178:181], v[144:147], v[20:35]
	v_exp_f32_e32 v68, v68
	v_exp_f32_e32 v69, v69
	v_mfma_f32_32x32x16_bf16 v[4:19], v[186:189], v[144:147], v[4:19]
	v_exp_f32_e32 v70, v70
	v_exp_f32_e32 v71, v71
	v_mfma_f32_32x32x16_bf16 v[20:35], v[182:185], v[140:143], v[20:35]
	v_exp_f32_e32 v72, v72
	v_exp_f32_e32 v73, v73
	v_mfma_f32_32x32x16_bf16 v[4:19], v[190:193], v[140:143], v[4:19]
	v_exp_f32_e32 v74, v74
	v_exp_f32_e32 v75, v75
	s_waitcnt lgkmcnt(6)
	v_mfma_f32_32x32x16_bf16 v[52:67], v[100:103], v[144:147], v[52:67]
	v_exp_f32_e32 v76, v76
	v_exp_f32_e32 v77, v77
	s_waitcnt lgkmcnt(2)
	v_mfma_f32_32x32x16_bf16 v[36:51], v[108:111], v[144:147], v[36:51]
	v_exp_f32_e32 v78, v78
	v_exp_f32_e32 v79, v79
	ds_read_b64_tr_b16 v[100:101], v152 offset:24576
	ds_read_b64_tr_b16 v[102:103], v177 offset:24576
	ds_read_b64_tr_b16 v[108:109], v194 offset:24576
	ds_read_b64_tr_b16 v[110:111], v195 offset:24576
	ds_read_b64_tr_b16 v[178:179], v196 offset:24576
	ds_read_b64_tr_b16 v[180:181], v197 offset:24576
	ds_read_b64_tr_b16 v[186:187], v202 offset:24576
	ds_read_b64_tr_b16 v[188:189], v203 offset:24576
	s_waitcnt lgkmcnt(8)
	v_mfma_f32_32x32x16_bf16 v[52:67], v[104:107], v[140:143], v[52:67]
	v_exp_f32_e32 v80, v80
	v_exp_f32_e32 v81, v81
	v_mfma_f32_32x32x16_bf16 v[36:51], v[112:115], v[140:143], v[36:51]
	v_exp_f32_e32 v82, v82
	v_exp_f32_e32 v83, v83
	ds_read_b64_tr_b16 v[104:105], v152 offset:28672
	ds_read_b64_tr_b16 v[106:107], v177 offset:28672
	ds_read_b64_tr_b16 v[112:113], v194 offset:28672
	ds_read_b64_tr_b16 v[114:115], v195 offset:28672
	ds_read_b64_tr_b16 v[182:183], v196 offset:28672
	ds_read_b64_tr_b16 v[184:185], v197 offset:28672
	ds_read_b64_tr_b16 v[190:191], v202 offset:28672
	ds_read_b64_tr_b16 v[192:193], v203 offset:28672
	s_waitcnt lgkmcnt(14)
	v_mfma_f32_32x32x16_bf16 v[52:67], v[100:103], v[132:135], v[52:67]
	v_exp_f32_e32 v84, v84
	v_exp_f32_e32 v85, v85
	v_pk_add_f32 v[220:221], v[68:69], v[70:71]
	v_pk_add_f32 v[222:223], v[72:73], v[74:75]
	s_waitcnt lgkmcnt(12)
	v_mfma_f32_32x32x16_bf16 v[36:51], v[108:111], v[132:135], v[36:51]
	v_exp_f32_e32 v86, v86
	v_exp_f32_e32 v87, v87
	v_pk_add_f32 v[224:225], v[76:77], v[78:79]
	v_pk_add_f32 v[226:227], v[80:81], v[82:83]
	s_waitcnt lgkmcnt(10)
	v_mfma_f32_32x32x16_bf16 v[20:35], v[178:181], v[132:135], v[20:35]
	v_exp_f32_e32 v88, v88
	v_exp_f32_e32 v89, v89
	v_pk_add_f32 v[220:221], v[220:221], v[222:223]
	v_pk_add_f32 v[224:225], v[224:225], v[226:227]
	s_waitcnt lgkmcnt(8)
	v_mfma_f32_32x32x16_bf16 v[4:19], v[186:189], v[132:135], v[4:19]
	v_exp_f32_e32 v90, v90
	v_exp_f32_e32 v91, v91
	v_pk_add_f32 v[220:221], v[220:221], v[224:225]
	s_waitcnt lgkmcnt(6)
	v_mfma_f32_32x32x16_bf16 v[52:67], v[104:107], v[136:139], v[52:67]
	v_exp_f32_e32 v92, v92
	v_exp_f32_e32 v93, v93
	v_pk_add_f32 v[222:223], v[84:85], v[86:87]
	v_pk_add_f32 v[224:225], v[88:89], v[90:91]
	s_waitcnt lgkmcnt(4)
	v_mfma_f32_32x32x16_bf16 v[36:51], v[112:115], v[136:139], v[36:51]
	v_exp_f32_e32 v94, v94
	v_exp_f32_e32 v95, v95
	v_pk_add_f32 v[222:223], v[222:223], v[224:225]
	s_waitcnt lgkmcnt(2)
	v_mfma_f32_32x32x16_bf16 v[20:35], v[182:185], v[136:139], v[20:35]
	v_exp_f32_e32 v96, v96
	v_exp_f32_e32 v97, v97
	v_pk_add_f32 v[220:221], v[220:221], v[222:223]
	s_waitcnt lgkmcnt(0)
	v_mfma_f32_32x32x16_bf16 v[4:19], v[190:193], v[136:139], v[4:19]
	v_exp_f32_e32 v98, v98
	v_exp_f32_e32 v99, v99
	s_andn2_b64 vcc, exec, s[78:79]
	s_cbranch_vccnz .LBB0_439
	v_pk_add_f32 v[222:223], v[92:93], v[94:95]
	v_pk_add_f32 v[224:225], v[96:97], v[98:99]
	v_pk_add_f32 v[222:223], v[222:223], v[224:225]
	v_pk_add_f32 v[220:221], v[220:221], v[222:223]
	s_nop 0
	v_add_f32_e32 v152, v220, v221
	s_branch .Latt_sum_done

.Latt_sum_done:
	s_mov_b32 s0, 0x46000000
	v_cmp_nge_f32_e32 vcc, s0, v152
	s_cbranch_vccz .LBB0_438
	v_max_f32_e32 v100, v69, v69
	v_max_f32_e32 v101, v68, v68
	v_max_f32_e32 v100, v101, v100
	v_max_f32_e32 v101, v71, v71
	v_max_f32_e32 v102, v70, v70
	v_max_f32_e32 v101, v102, v101
	v_max_f32_e32 v102, v75, v75
	v_max_f32_e32 v103, v74, v74
	v_max_f32_e32 v102, v103, v102
	v_max3_f32 v102, v72, v73, v102
	v_max3_f32 v100, v100, v101, v102
	v_max_f32_e32 v101, v77, v77
	v_max_f32_e32 v102, v76, v76
	v_max_f32_e32 v101, v102, v101
	v_max_f32_e32 v102, v79, v79
	v_max_f32_e32 v103, v78, v78
	v_max_f32_e32 v102, v103, v102
	v_max_f32_e32 v103, v83, v83
	v_max_f32_e32 v104, v82, v82
	v_max_f32_e32 v103, v104, v103
	v_max3_f32 v103, v80, v81, v103
	v_max3_f32 v101, v101, v102, v103
	v_max_f32_e32 v102, v87, v87
	v_max_f32_e32 v103, v86, v86
	v_max_f32_e32 v102, v103, v102
	v_max_f32_e32 v103, v91, v91
	v_max_f32_e32 v104, v90, v90
	v_max_f32_e32 v103, v104, v103
	v_max_f32_e32 v104, v93, v93
	v_max_f32_e32 v105, v92, v92
	v_max_f32_e32 v104, v105, v104
	v_max_f32_e32 v105, v95, v95
	v_max_f32_e32 v106, v94, v94
	v_max_f32_e32 v105, v106, v105
	v_max_f32_e32 v106, v99, v99
	v_max_f32_e32 v107, v98, v98
	v_max_f32_e32 v106, v107, v106
	v_max3_f32 v106, v96, v97, v106
	v_max3_f32 v102, v84, v85, v102
	v_max3_f32 v103, v88, v89, v103
	v_max3_f32 v104, v104, v105, v106
	v_max3_f32 v102, v102, v103, v104
	v_max3_f32 v100, v100, v101, v102
	v_mov_b32_e32 v101, v100
	s_nop 1
	v_permlane32_swap_b32 v101, v100
	s_nop 1
	s_nop 0
	v_max3_f32 v101, v101, v100, 1.0
	v_rcp_f32_e32 v100, v101
	s_nop 0
	v_pk_mul_f32 v[66:67], v[66:67], v[100:101] op_sel_hi:[1,0]
	v_pk_mul_f32 v[64:65], v[64:65], v[100:101] op_sel_hi:[1,0]
	v_pk_mul_f32 v[62:63], v[62:63], v[100:101] op_sel_hi:[1,0]
	v_pk_mul_f32 v[60:61], v[60:61], v[100:101] op_sel_hi:[1,0]
	v_pk_mul_f32 v[58:59], v[58:59], v[100:101] op_sel_hi:[1,0]
	v_pk_mul_f32 v[56:57], v[56:57], v[100:101] op_sel_hi:[1,0]
	v_pk_mul_f32 v[54:55], v[54:55], v[100:101] op_sel_hi:[1,0]
	v_pk_mul_f32 v[52:53], v[52:53], v[100:101] op_sel_hi:[1,0]
	v_pk_mul_f32 v[50:51], v[50:51], v[100:101] op_sel_hi:[1,0]
	v_pk_mul_f32 v[48:49], v[48:49], v[100:101] op_sel_hi:[1,0]
	v_pk_mul_f32 v[46:47], v[46:47], v[100:101] op_sel_hi:[1,0]
	v_pk_mul_f32 v[44:45], v[44:45], v[100:101] op_sel_hi:[1,0]
	v_pk_mul_f32 v[42:43], v[42:43], v[100:101] op_sel_hi:[1,0]
	v_pk_mul_f32 v[40:41], v[40:41], v[100:101] op_sel_hi:[1,0]
	v_pk_mul_f32 v[38:39], v[38:39], v[100:101] op_sel_hi:[1,0]
	v_pk_mul_f32 v[36:37], v[36:37], v[100:101] op_sel_hi:[1,0]
	v_pk_mul_f32 v[34:35], v[34:35], v[100:101] op_sel_hi:[1,0]
	v_pk_mul_f32 v[32:33], v[32:33], v[100:101] op_sel_hi:[1,0]
	v_pk_mul_f32 v[30:31], v[30:31], v[100:101] op_sel_hi:[1,0]
	v_pk_mul_f32 v[28:29], v[28:29], v[100:101] op_sel_hi:[1,0]
	v_pk_mul_f32 v[26:27], v[26:27], v[100:101] op_sel_hi:[1,0]
	v_pk_mul_f32 v[24:25], v[24:25], v[100:101] op_sel_hi:[1,0]
	v_pk_mul_f32 v[22:23], v[22:23], v[100:101] op_sel_hi:[1,0]
	v_pk_mul_f32 v[20:21], v[20:21], v[100:101] op_sel_hi:[1,0]
	v_pk_mul_f32 v[18:19], v[18:19], v[100:101] op_sel_hi:[1,0]
	v_pk_mul_f32 v[16:17], v[16:17], v[100:101] op_sel_hi:[1,0]
	v_pk_mul_f32 v[14:15], v[14:15], v[100:101] op_sel_hi:[1,0]
	v_pk_mul_f32 v[12:13], v[12:13], v[100:101] op_sel_hi:[1,0]
	v_pk_mul_f32 v[10:11], v[10:11], v[100:101] op_sel_hi:[1,0]
	v_pk_mul_f32 v[8:9], v[8:9], v[100:101] op_sel_hi:[1,0]
	v_pk_mul_f32 v[6:7], v[6:7], v[100:101] op_sel_hi:[1,0]
	v_pk_mul_f32 v[4:5], v[4:5], v[100:101] op_sel_hi:[1,0]
	v_log_f32_e32 v101, v101
	s_nop 0
	v_pk_mul_f32 v[82:83], v[82:83], v[100:101] op_sel_hi:[1,0]
	v_pk_mul_f32 v[80:81], v[80:81], v[100:101] op_sel_hi:[1,0]
	v_pk_mul_f32 v[78:79], v[78:79], v[100:101] op_sel_hi:[1,0]
	v_pk_mul_f32 v[76:77], v[76:77], v[100:101] op_sel_hi:[1,0]
	v_pk_mul_f32 v[74:75], v[74:75], v[100:101] op_sel_hi:[1,0]
	v_pk_mul_f32 v[72:73], v[72:73], v[100:101] op_sel_hi:[1,0]
	v_pk_mul_f32 v[70:71], v[70:71], v[100:101] op_sel_hi:[1,0]
	v_pk_mul_f32 v[68:69], v[68:69], v[100:101] op_sel_hi:[1,0]
	v_pk_mul_f32 v[98:99], v[98:99], v[100:101] op_sel_hi:[1,0]
	v_pk_mul_f32 v[96:97], v[96:97], v[100:101] op_sel_hi:[1,0]
	v_pk_mul_f32 v[94:95], v[94:95], v[100:101] op_sel_hi:[1,0]
	v_pk_mul_f32 v[92:93], v[92:93], v[100:101] op_sel_hi:[1,0]
	v_pk_mul_f32 v[90:91], v[90:91], v[100:101] op_sel_hi:[1,0]
	v_pk_mul_f32 v[88:89], v[88:89], v[100:101] op_sel_hi:[1,0]
	v_pk_mul_f32 v[86:87], v[86:87], v[100:101] op_sel_hi:[1,0]
	v_pk_mul_f32 v[84:85], v[84:85], v[100:101] op_sel_hi:[1,0]
	v_add_f32_e32 v167, v167, v101
	v_pk_mul_f32 v[152:153], v[152:153], v[100:101] op_sel_hi:[1,0]
